# speedup vs baseline: 1.0192x; 1.0104x over previous
.Lmk_nosplit_a:
	v_mfma_f32_32x32x64_f8f6f4 v[48:63], v[36:41], v[108:113], v[48:63] cbsz:2 blgp:2
	ds_read_b128 v[36:39], v124 offset:9216
	v_exp_f32_e32 v84, v84
	v_exp_f32_e32 v85, v85
	v_exp_f32_e32 v86, v86
	v_exp_f32_e32 v87, v87
	v_pk_add_f32 v[120:121], v[120:121], v[80:81]
	v_pk_add_f32 v[122:123], v[122:123], v[82:83]
	v_mfma_f32_32x32x64_f8f6f4 v[48:63], v[42:47], v[114:119], v[48:63] cbsz:2 blgp:2
	ds_read_b128 v[40:43], v124 offset:10240
	ds_read_b128 v[44:47], v124 offset:11264
	v_exp_f32_e32 v88, v88
	v_exp_f32_e32 v89, v89
	v_exp_f32_e32 v90, v90
	v_exp_f32_e32 v91, v91
	v_pk_add_f32 v[120:121], v[120:121], v[84:85]
	v_pk_add_f32 v[122:123], v[122:123], v[86:87]
	s_waitcnt lgkmcnt(6)
	v_mfma_f32_32x32x64_f8f6f4 v[64:79], v[0:5], v[96:101], 0 cbsz:2 blgp:2
	v_exp_f32_e32 v92, v92
	v_exp_f32_e32 v93, v93
	v_exp_f32_e32 v94, v94
	v_exp_f32_e32 v95, v95
	v_pk_add_f32 v[120:121], v[120:121], v[88:89]
	v_pk_add_f32 v[122:123], v[122:123], v[90:91]
	v_mfma_f32_32x32x64_f8f6f4 v[64:79], v[6:11], v[102:107], v[64:79] cbsz:2 blgp:2
	v_exp_f32_e32 v48, v48
	v_exp_f32_e32 v49, v49
	v_exp_f32_e32 v50, v50
	v_exp_f32_e32 v51, v51
	v_pk_add_f32 v[120:121], v[120:121], v[92:93]
	v_pk_add_f32 v[122:123], v[122:123], v[94:95]
	v_mfma_f32_32x32x64_f8f6f4 v[64:79], v[12:17], v[108:113], v[64:79] cbsz:2 blgp:2
	v_exp_f32_e32 v52, v52
	v_exp_f32_e32 v53, v53
	v_exp_f32_e32 v54, v54
	v_exp_f32_e32 v55, v55
	v_pk_add_f32 v[120:121], v[120:121], v[48:49]
	v_pk_add_f32 v[122:123], v[122:123], v[50:51]
	v_mfma_f32_32x32x64_f8f6f4 v[64:79], v[18:23], v[114:119], v[64:79] cbsz:2 blgp:2
	v_exp_f32_e32 v56, v56
	v_exp_f32_e32 v57, v57
	v_exp_f32_e32 v58, v58
	v_exp_f32_e32 v59, v59
	v_pk_add_f32 v[120:121], v[120:121], v[52:53]
	v_pk_add_f32 v[122:123], v[122:123], v[54:55]
	s_waitcnt lgkmcnt(0)
	v_mfma_f32_32x32x64_f8f6f4 v[80:95], v[24:29], v[96:101], 0 cbsz:2 blgp:2
	v_exp_f32_e32 v60, v60
	v_exp_f32_e32 v61, v61
	v_exp_f32_e32 v62, v62
	v_exp_f32_e32 v63, v63
	v_pk_add_f32 v[120:121], v[120:121], v[56:57]
	v_pk_add_f32 v[122:123], v[122:123], v[58:59]
	v_mfma_f32_32x32x64_f8f6f4 v[80:95], v[30:35], v[102:107], v[80:95] cbsz:2 blgp:2
	v_exp_f32_e32 v64, v64
	v_exp_f32_e32 v65, v65
	v_exp_f32_e32 v66, v66
	v_exp_f32_e32 v67, v67
	v_pk_add_f32 v[120:121], v[120:121], v[60:61]
	v_pk_add_f32 v[122:123], v[122:123], v[62:63]
	v_mfma_f32_32x32x64_f8f6f4 v[80:95], v[36:41], v[108:113], v[80:95] cbsz:2 blgp:2
	v_exp_f32_e32 v68, v68
	v_exp_f32_e32 v69, v69
	v_exp_f32_e32 v70, v70
	v_exp_f32_e32 v71, v71
	v_pk_add_f32 v[120:121], v[120:121], v[64:65]
	v_pk_add_f32 v[122:123], v[122:123], v[66:67]
	v_mfma_f32_32x32x64_f8f6f4 v[80:95], v[42:47], v[114:119], v[80:95] cbsz:2 blgp:2
	v_exp_f32_e32 v72, v72
	v_exp_f32_e32 v73, v73
	v_exp_f32_e32 v74, v74
	v_exp_f32_e32 v75, v75
	v_pk_add_f32 v[120:121], v[120:121], v[68:69]
	v_pk_add_f32 v[122:123], v[122:123], v[70:71]
	v_exp_f32_e32 v76, v76
	v_exp_f32_e32 v77, v77
	v_exp_f32_e32 v78, v78
	v_exp_f32_e32 v79, v79
	v_pk_add_f32 v[120:121], v[120:121], v[72:73]
	v_pk_add_f32 v[122:123], v[122:123], v[74:75]
	s_nop 1
	v_exp_f32_e32 v80, v80
	v_exp_f32_e32 v81, v81
	v_exp_f32_e32 v82, v82
	v_exp_f32_e32 v83, v83
	v_pk_add_f32 v[120:121], v[120:121], v[76:77]
	v_pk_add_f32 v[122:123], v[122:123], v[78:79]
	v_exp_f32_e32 v84, v84
	v_exp_f32_e32 v85, v85
	v_exp_f32_e32 v86, v86
	v_exp_f32_e32 v87, v87
	v_pk_add_f32 v[120:121], v[120:121], v[80:81]
	v_pk_add_f32 v[122:123], v[122:123], v[82:83]
	v_exp_f32_e32 v88, v88
	v_exp_f32_e32 v89, v89
	v_exp_f32_e32 v90, v90
	v_exp_f32_e32 v91, v91
	v_pk_add_f32 v[120:121], v[120:121], v[84:85]
	v_pk_add_f32 v[122:123], v[122:123], v[86:87]
	v_exp_f32_e32 v92, v92
	v_exp_f32_e32 v93, v93
	v_exp_f32_e32 v94, v94
	v_exp_f32_e32 v95, v95
	v_pk_add_f32 v[120:121], v[120:121], v[88:89]
	v_pk_add_f32 v[122:123], v[122:123], v[90:91]
	v_pk_add_f32 v[120:121], v[120:121], v[92:93]
	v_pk_add_f32 v[122:123], v[122:123], v[94:95]
	v_add_f32_e32 v120, v120, v121
	v_add_f32_e32 v122, v122, v123
	v_lshrrev_b32_e32 v126, 2, v124
	v_add_f32_e32 v120, v120, v122
	v_mov_b32_e32 v123, v127
	v_mov_b32_e32 v122, v120
	s_mov_b64 s[4:5], s[30:31]
	s_mov_b64 s[6:7], s[32:33]
	s_lshl_b32 s14, s14, 7
	v_add_u32_e32 v126, s14, v126
	s_nop 1
	v_permlane32_swap_b32_e32 v120, v122
	v_permlane32_swap_b32_e32 v127, v123
	s_nop 1
	v_add_f32_e32 v120, v120, v122
	v_add_f32_e32 v127, v127, v123
	v_cmp_gt_u32_e32 vcc, 0x200, v124
	s_and_saveexec_b64 s[16:17], vcc
	s_cbranch_execz .Lmk_end_a
	s_cmp_lt_u32 s8, 10
	s_cbranch_scc1 .Lmk_pos_only_a
	s_cmp_eq_u32 s8, 10
	s_cbranch_scc0 .Lmk_neg_only_a
	global_atomic_add_f32 v126, v127, s[4:5]

.Lmk_nosplit_b:
	v_mfma_f32_32x32x64_f8f6f4 v[48:63], v[36:41], v[108:113], v[48:63] cbsz:2 blgp:2
	ds_read_b128 v[36:39], v124 offset:9216
	v_exp_f32_e32 v84, v84
	v_exp_f32_e32 v85, v85
	v_exp_f32_e32 v86, v86
	v_exp_f32_e32 v87, v87
	v_pk_add_f32 v[120:121], v[120:121], v[80:81]
	v_pk_add_f32 v[122:123], v[122:123], v[82:83]
	v_mfma_f32_32x32x64_f8f6f4 v[48:63], v[42:47], v[114:119], v[48:63] cbsz:2 blgp:2
	ds_read_b128 v[40:43], v124 offset:10240
	ds_read_b128 v[44:47], v124 offset:11264
	v_exp_f32_e32 v88, v88
	v_exp_f32_e32 v89, v89
	v_exp_f32_e32 v90, v90
	v_exp_f32_e32 v91, v91
	v_pk_add_f32 v[120:121], v[120:121], v[84:85]
	v_pk_add_f32 v[122:123], v[122:123], v[86:87]
	s_setprio 0
	s_waitcnt lgkmcnt(6)
	v_mfma_f32_32x32x64_f8f6f4 v[64:79], v[0:5], v[96:101], 0 cbsz:2 blgp:2
	v_exp_f32_e32 v92, v92
	v_exp_f32_e32 v93, v93
	v_exp_f32_e32 v94, v94
	v_exp_f32_e32 v95, v95
	v_pk_add_f32 v[120:121], v[120:121], v[88:89]
	v_pk_add_f32 v[122:123], v[122:123], v[90:91]
	v_mfma_f32_32x32x64_f8f6f4 v[64:79], v[6:11], v[102:107], v[64:79] cbsz:2 blgp:2
	v_exp_f32_e32 v48, v48
	v_exp_f32_e32 v49, v49
	v_exp_f32_e32 v50, v50
	v_exp_f32_e32 v51, v51
	v_pk_add_f32 v[120:121], v[120:121], v[92:93]
	v_pk_add_f32 v[122:123], v[122:123], v[94:95]
	v_mfma_f32_32x32x64_f8f6f4 v[64:79], v[12:17], v[108:113], v[64:79] cbsz:2 blgp:2
	v_exp_f32_e32 v52, v52
	v_exp_f32_e32 v53, v53
	v_exp_f32_e32 v54, v54
	v_exp_f32_e32 v55, v55
	v_pk_add_f32 v[120:121], v[120:121], v[48:49]
	v_pk_add_f32 v[122:123], v[122:123], v[50:51]
	v_mfma_f32_32x32x64_f8f6f4 v[64:79], v[18:23], v[114:119], v[64:79] cbsz:2 blgp:2
	v_exp_f32_e32 v56, v56
	v_exp_f32_e32 v57, v57
	v_exp_f32_e32 v58, v58
	v_exp_f32_e32 v59, v59
	v_pk_add_f32 v[120:121], v[120:121], v[52:53]
	v_pk_add_f32 v[122:123], v[122:123], v[54:55]
	s_waitcnt lgkmcnt(0)
	v_mfma_f32_32x32x64_f8f6f4 v[80:95], v[24:29], v[96:101], 0 cbsz:2 blgp:2
	v_exp_f32_e32 v60, v60
	v_exp_f32_e32 v61, v61
	v_exp_f32_e32 v62, v62
	v_exp_f32_e32 v63, v63
	v_pk_add_f32 v[120:121], v[120:121], v[56:57]
	v_pk_add_f32 v[122:123], v[122:123], v[58:59]
	v_mfma_f32_32x32x64_f8f6f4 v[80:95], v[30:35], v[102:107], v[80:95] cbsz:2 blgp:2
	v_exp_f32_e32 v64, v64
	v_exp_f32_e32 v65, v65
	v_exp_f32_e32 v66, v66
	v_exp_f32_e32 v67, v67
	v_pk_add_f32 v[120:121], v[120:121], v[60:61]
	v_pk_add_f32 v[122:123], v[122:123], v[62:63]
	v_mfma_f32_32x32x64_f8f6f4 v[80:95], v[36:41], v[108:113], v[80:95] cbsz:2 blgp:2
	v_exp_f32_e32 v68, v68
	v_exp_f32_e32 v69, v69
	v_exp_f32_e32 v70, v70
	v_exp_f32_e32 v71, v71
	v_pk_add_f32 v[120:121], v[120:121], v[64:65]
	v_pk_add_f32 v[122:123], v[122:123], v[66:67]
	v_mfma_f32_32x32x64_f8f6f4 v[80:95], v[42:47], v[114:119], v[80:95] cbsz:2 blgp:2
	v_exp_f32_e32 v72, v72
	v_exp_f32_e32 v73, v73
	v_exp_f32_e32 v74, v74
	v_exp_f32_e32 v75, v75
	v_pk_add_f32 v[120:121], v[120:121], v[68:69]
	v_pk_add_f32 v[122:123], v[122:123], v[70:71]
	v_exp_f32_e32 v76, v76
	v_exp_f32_e32 v77, v77
	v_exp_f32_e32 v78, v78
	v_exp_f32_e32 v79, v79
	v_pk_add_f32 v[120:121], v[120:121], v[72:73]
	v_pk_add_f32 v[122:123], v[122:123], v[74:75]
	s_nop 1
	v_exp_f32_e32 v80, v80
	v_exp_f32_e32 v81, v81
	v_exp_f32_e32 v82, v82
	v_exp_f32_e32 v83, v83
	v_pk_add_f32 v[120:121], v[120:121], v[76:77]
	v_pk_add_f32 v[122:123], v[122:123], v[78:79]
	v_exp_f32_e32 v84, v84
	v_exp_f32_e32 v85, v85
	v_exp_f32_e32 v86, v86
	v_exp_f32_e32 v87, v87
	v_pk_add_f32 v[120:121], v[120:121], v[80:81]
	v_pk_add_f32 v[122:123], v[122:123], v[82:83]
	v_exp_f32_e32 v88, v88
	v_exp_f32_e32 v89, v89
	v_exp_f32_e32 v90, v90
	v_exp_f32_e32 v91, v91
	v_pk_add_f32 v[120:121], v[120:121], v[84:85]
	v_pk_add_f32 v[122:123], v[122:123], v[86:87]
	v_exp_f32_e32 v92, v92
	v_exp_f32_e32 v93, v93
	v_exp_f32_e32 v94, v94
	v_exp_f32_e32 v95, v95
	v_pk_add_f32 v[120:121], v[120:121], v[88:89]
	v_pk_add_f32 v[122:123], v[122:123], v[90:91]
	v_pk_add_f32 v[120:121], v[120:121], v[92:93]
	v_pk_add_f32 v[122:123], v[122:123], v[94:95]
	v_add_f32_e32 v120, v120, v121
	v_add_f32_e32 v122, v122, v123
	v_lshrrev_b32_e32 v126, 2, v124
	v_add_f32_e32 v120, v120, v122
	v_mov_b32_e32 v123, v127
	v_mov_b32_e32 v122, v120
	s_mov_b64 s[4:5], s[30:31]
	s_mov_b64 s[6:7], s[32:33]
	s_lshl_b32 s14, s14, 7
	v_add_u32_e32 v126, s14, v126
	s_nop 1
	v_permlane32_swap_b32_e32 v120, v122
	v_permlane32_swap_b32_e32 v127, v123
	s_nop 1
	v_add_f32_e32 v120, v120, v122
	v_add_f32_e32 v127, v127, v123
	v_cmp_gt_u32_e32 vcc, 0x200, v124
	s_and_saveexec_b64 s[16:17], vcc
	s_cbranch_execz .Lmk_end_b
	s_cmp_lt_u32 s8, 10
	s_cbranch_scc1 .Lmk_pos_only_b
	s_cmp_eq_u32 s8, 10
	s_cbranch_scc0 .Lmk_neg_only_b
	global_atomic_add_f32 v126, v127, s[4:5]
